# occ3lin
# speedup vs baseline: 1.0560x; 1.0421x over previous
	.amdhsa_kernel _Z10gae_kernelPKfPKiS2_S0_S0_S0_PfS3_
		.amdhsa_group_segment_fixed_size 54016
		.amdhsa_private_segment_fixed_size 0
		.amdhsa_kernarg_size 64
		.amdhsa_user_sgpr_count 2
		.amdhsa_user_sgpr_dispatch_ptr 0
		.amdhsa_user_sgpr_queue_ptr 0
		.amdhsa_user_sgpr_kernarg_segment_ptr 1
		.amdhsa_user_sgpr_dispatch_id 0
		.amdhsa_user_sgpr_kernarg_preload_length 0
		.amdhsa_user_sgpr_kernarg_preload_offset 0
		.amdhsa_user_sgpr_private_segment_size 0
		.amdhsa_uses_dynamic_stack 0
		.amdhsa_enable_private_segment 0
		.amdhsa_system_sgpr_workgroup_id_x 1
		.amdhsa_system_sgpr_workgroup_id_y 0
		.amdhsa_system_sgpr_workgroup_id_z 0
		.amdhsa_system_sgpr_workgroup_info 0
		.amdhsa_system_vgpr_workitem_id 0
		.amdhsa_next_free_vgpr 80
		.amdhsa_next_free_sgpr 96
		.amdhsa_accum_offset 76
		.amdhsa_reserve_vcc 1
		.amdhsa_float_round_mode_32 0
		.amdhsa_float_round_mode_16_64 0
		.amdhsa_float_denorm_mode_32 3
		.amdhsa_float_denorm_mode_16_64 3
		.amdhsa_dx10_clamp 1
		.amdhsa_ieee_mode 1
		.amdhsa_fp16_overflow 0
		.amdhsa_tg_split 0
		.amdhsa_exception_fp_ieee_invalid_op 0
		.amdhsa_exception_fp_denorm_src 0
		.amdhsa_exception_fp_ieee_div_zero 0
		.amdhsa_exception_fp_ieee_overflow 0
		.amdhsa_exception_fp_ieee_underflow 0
		.amdhsa_exception_fp_ieee_inexact 0
		.amdhsa_exception_int_div_zero 0
	.end_amdhsa_kernel

amdhsa.kernels:
  - .agpr_count:     0
    .args:
      - .actual_access:  read_only
        .address_space:  global
        .offset:         0
        .size:           8
        .value_kind:     global_buffer
      - .actual_access:  read_only
        .address_space:  global
        .offset:         8
        .size:           8
        .value_kind:     global_buffer
      - .actual_access:  read_only
        .address_space:  global
        .offset:         16
        .size:           8
        .value_kind:     global_buffer
      - .actual_access:  read_only
        .address_space:  global
        .offset:         24
        .size:           8
        .value_kind:     global_buffer
      - .actual_access:  read_only
        .address_space:  global
        .offset:         32
        .size:           8
        .value_kind:     global_buffer
      - .actual_access:  read_only
        .address_space:  global
        .offset:         40
        .size:           8
        .value_kind:     global_buffer
      - .actual_access:  write_only
        .address_space:  global
        .offset:         48
        .size:           8
        .value_kind:     global_buffer
      - .actual_access:  write_only
        .address_space:  global
        .offset:         56
        .size:           8
        .value_kind:     global_buffer
    .group_segment_fixed_size: 54016
    .kernarg_segment_align: 8
    .kernarg_segment_size: 64
    .language:       OpenCL C
    .language_version:
      - 2
      - 0
    .max_flat_workgroup_size: 256
    .name:           _Z10gae_kernelPKfPKiS2_S0_S0_S0_PfS3_
    .private_segment_fixed_size: 0
    .sgpr_count:     22
    .sgpr_spill_count: 0
    .symbol:         _Z10gae_kernelPKfPKiS2_S0_S0_S0_PfS3_.kd
    .uniform_work_group_size: 1
    .uses_dynamic_stack: false
    .vgpr_count:     74
    .vgpr_spill_count: 0
    .wavefront_size: 64
